# baseline (speedup 1.0000x reference)
_Z11attn_kernelPKDF16_S0_S0_PfPDF16_S1_:
	s_lshl_b32 s3, s2, 7
	s_lshr_b32 s4, s2, 2
	s_and_b32 s3, s3, 0x180
	s_and_b32 s4, s4, 0x3ffffffe
	s_add_i32 s3, s3, s4
	s_bfe_u32 s2, s2, 0x10002
	s_or_b32 s40, s3, s2
	s_mov_b32 s41, 0
	s_lshl_b64 s[2:3], s[40:41], 2
	s_getpc_b64 s[4:5]
	s_add_u32 s4, s4, g_tab@rel32@lo+4
	s_addc_u32 s5, s5, g_tab@rel32@hi+12
	s_add_u32 s42, s4, s2
	s_addc_u32 s43, s5, s3
	s_load_dword s12, s[42:43], 0x0
	s_load_dwordx4 s[4:7], s[0:1], 0x8
	s_load_dword s76, s[42:43], 0x1000
	s_load_dwordx2 s[80:81], s[0:1], 0x0
	s_load_dwordx4 s[84:87], s[0:1], 0x18
	s_load_dwordx2 s[88:89], s[0:1], 0x28
	v_lshlrev_b32_e32 v2, 4, v0
	s_movk_i32 s8, 0x70
	v_readfirstlane_b32 s3, v0
	s_waitcnt lgkmcnt(0)
	s_add_u32 s70, s4, 0x2000
	s_addc_u32 s71, s5, 0
	s_add_u32 s72, s6, 0x2000
	s_addc_u32 s73, s7, 0
	s_and_b32 s2, s12, 3
	s_lshl_b32 s10, s2, 19
	v_bitop3_b32 v10, v2, s8, v0 bitop3:0x48
	s_add_u32 s8, s6, s10
	s_addc_u32 s9, s7, 0
	s_lshr_b32 s13, s3, 6
	s_bfe_u32 s40, s12, 0x70007
	s_bfe_u32 s33, s12, 0x6000e
	v_and_b32_e32 v1, 0x1f80, v2
	s_add_u32 s10, s4, s10
	v_or_b32_e32 v50, v10, v1
	v_mov_b32_e32 v51, 0
	s_addc_u32 s11, s5, 0
	v_lshl_add_u64 v[52:53], s[10:11], 0, v[50:51]
	v_lshl_add_u64 v[54:55], s[8:9], 0, v[50:51]
	s_lshl_b32 s8, s40, 13
	s_mov_b32 s9, s41
	s_lshl_b32 s50, s13, 10
	v_lshl_add_u64 v[2:3], v[52:53], 0, s[8:9]
	s_mov_b32 m0, s50
	s_add_i32 s51, s50, 0x2000
	global_load_lds_dwordx4 v[2:3], off
	v_lshl_add_u64 v[2:3], v[54:55], 0, s[8:9]
	s_mov_b32 m0, s51
	s_cmp_eq_u32 s33, 0
	global_load_lds_dwordx4 v[2:3], off
	s_cbranch_scc1 .LBB2_30
	s_mov_b64 s[14:15], s[80:81]
	s_mov_b64 s[8:9], s[84:85]
	s_mov_b64 s[10:11], s[86:87]
	s_mov_b64 s[44:45], s[88:89]
	s_cmp_ge_u32 s13, 4
	s_cbranch_scc1 .Lattn_prio_done
	s_setprio 1
